# cross-section code prefetch windows widened by 512 B so they still cover the target if the layout shifts
# speedup vs baseline: 1.0035x; 1.0015x over previous
.LBB0_6:
	s_or_b64 exec, exec, s[4:5]
	s_waitcnt lgkmcnt(0)
	s_barrier
	ds_read_b32 v19, v29
	v_lshl_add_u32 v26, v26, s8, v27
	ds_read_b32 v27, v30
	ds_read_b32 v28, v28
	ds_read_b32 v25, v25
	s_waitcnt vmcnt(3)
	v_cmp_eq_u32_e32 vcc, 0, v17
	s_mov_b64 s[4:5], -1
	s_waitcnt lgkmcnt(3)
	v_add_lshl_u32 v19, v26, v19, 2
	ds_write2st64_b32 v19, v8, v9 offset1:64
	v_bfrev_b32_e32 v8, 1
	v_cndmask_b32_e32 v8, 0, v8, vcc
	v_or_b32_e32 v8, v8, v0
	ds_write_b32 v19, v8 offset:32768
	v_lshl_add_u32 v8, v20, s8, v21
	s_waitcnt lgkmcnt(4)
	v_add_lshl_u32 v8, v8, v27, 2
	ds_write2st64_b32 v8, v4, v5 offset1:64
	v_mov_b32_e32 v4, 0x400
	v_mov_b32_e32 v5, 0x80000400
	s_waitcnt vmcnt(2)
	v_cmp_eq_u32_e32 vcc, 0, v16
	s_nop 1
	v_cndmask_b32_e32 v4, v4, v5, vcc
	v_or_b32_e32 v4, v4, v0
	ds_write_b32 v8, v4 offset:32768
	v_lshl_add_u32 v4, v22, s8, v23
	s_waitcnt lgkmcnt(5)
	v_add_lshl_u32 v4, v4, v28, 2
	ds_write2st64_b32 v4, v6, v7 offset1:64
	v_mov_b32_e32 v5, 0x800
	v_mov_b32_e32 v6, 0x80000800
	s_waitcnt vmcnt(1)
	v_cmp_eq_u32_e32 vcc, 0, v15
	s_nop 1
	v_cndmask_b32_e32 v5, v5, v6, vcc
	v_or_b32_e32 v5, v5, v0
	ds_write_b32 v4, v5 offset:32768
	v_lshl_add_u32 v4, v24, s8, v18
	s_waitcnt lgkmcnt(6)
	v_add_lshl_u32 v4, v4, v25, 2
	ds_write2st64_b32 v4, v2, v3 offset1:64
	v_mov_b32_e32 v2, 0xc00
	v_mov_b32_e32 v3, 0x80000c00
	s_waitcnt vmcnt(0)
	v_cmp_eq_u32_e32 vcc, 0, v14
	s_nop 1
	v_cndmask_b32_e32 v2, v2, v3, vcc
	v_or_b32_e32 v2, v2, v0
	ds_write_b32 v4, v2 offset:32768
	s_waitcnt lgkmcnt(0)
	s_barrier
	s_getpc_b64 s[30:31]
	s_add_u32 s30, s30, 0x24b8
	s_addc_u32 s31, s31, 0
	v_lshlrev_b32_e32 v40, 6, v0
	v_min_u32_e32 v40, 0x2f00, v40
	global_load_dword v40, v40, s[30:31]
	s_and_b32 s32, s0, 0xfffff000
	s_mov_b32 s33, s1
	v_and_b32_e32 v41, 63, v0
	v_lshlrev_b32_e32 v41, 6, v41
	global_load_dword v41, v41, s[32:33]
	ds_read_b32 v14, v11 offset:32768
	s_mov_b64 s[18:19], s[44:45]
	s_mov_b64 s[8:9], s[36:37]
	s_mov_b64 s[10:11], s[38:39]
	s_mov_b64 s[12:13], s[40:41]
	s_mov_b64 s[14:15], s[42:43]
	ds_read2st64_b32 v[4:5], v11 offset1:64
	v_or_b32_e32 v2, s16, v0
	v_mov_b32_e32 v3, 0
	s_waitcnt lgkmcnt(0)
	v_and_b32_e32 v15, 0x7fffffff, v14
	s_and_b64 vcc, exec, s[2:3]
	v_lshlrev_b64 v[6:7], 2, v[2:3]
	s_cbranch_vccz .LBB0_8
	v_lshl_add_u64 v[8:9], s[10:11], 0, v[6:7]
	global_store_dword v[8:9], v4, off
	v_lshl_add_u64 v[8:9], s[12:13], 0, v[6:7]
	global_store_dword v[8:9], v5, off
	v_lshl_add_u64 v[8:9], s[14:15], 0, v[6:7]
	global_store_dword v[8:9], v15, off
	s_mov_b64 s[4:5], 0

.LBB4_39:
	s_waitcnt vmcnt(5)
	v_rcp_f32_e32 v2, v133
	s_waitcnt vmcnt(4)
	v_rcp_f32_e32 v3, v132
	s_waitcnt vmcnt(3)
	v_rcp_f32_e32 v4, v131
	v_cmp_lt_f32_e32 vcc, 0, v133
	s_waitcnt vmcnt(2)
	v_rcp_f32_e32 v5, v130
	s_waitcnt vmcnt(1)
	v_rcp_f32_e32 v6, v129
	v_cndmask_b32_e32 v2, 0, v2, vcc
	v_cmp_lt_f32_e32 vcc, 0, v132
	s_waitcnt vmcnt(0)
	v_rcp_f32_e32 v7, v128
	s_getpc_b64 s[36:37]
	s_sub_u32 s36, s36, 0x9440
	s_subb_u32 s37, s37, 0
	v_lshlrev_b32_e32 v183, 6, v0
	v_min_u32_e32 v183, 0x1d80, v183
	global_load_dword v183, v183, s[36:37]
	v_lshlrev_b32_e32 v182, 6, v38
	global_load_dword v182, v182, s[38:39]
	s_lshl_b32 s40, s29, 10
	s_add_u32 s40, s42, s40
	s_addc_u32 s41, s43, 0
	v_lshlrev_b32_e32 v181, 6, v0
	v_and_b32_e32 v181, 0x7fc0, v181
	global_load_dword v181, v181, s[40:41]
	s_mov_b32 s4, 0x42c80000
	v_cndmask_b32_e32 v3, 0, v3, vcc
	v_cmp_lt_f32_e32 vcc, 0, v131
	v_cmp_ngt_f32_e64 s[2:3], s4, v3
	s_mov_b64 s[6:7], 0
	v_cndmask_b32_e32 v4, 0, v4, vcc
	v_cmp_lt_f32_e32 vcc, 0, v130
	s_nop 1
	v_cndmask_b32_e32 v5, 0, v5, vcc
	v_cmp_lt_f32_e32 vcc, 0, v129
	s_nop 1
	v_cndmask_b32_e32 v6, 0, v6, vcc
	v_cmp_lt_f32_e32 vcc, 0, v128
	s_nop 1
	v_cndmask_b32_e32 v7, 0, v7, vcc
	v_cmp_ngt_f32_e32 vcc, s4, v2
	s_or_b64 s[2:3], vcc, s[2:3]
	v_cmp_ngt_f32_e32 vcc, s4, v4
	s_or_b64 s[2:3], s[2:3], vcc
	v_cmp_ngt_f32_e32 vcc, s4, v5
	s_or_b64 s[2:3], s[2:3], vcc
	v_cmp_ngt_f32_e32 vcc, s4, v6
	s_or_b64 s[2:3], s[2:3], vcc
	v_cmp_ngt_f32_e32 vcc, s4, v7
	s_or_b64 s[2:3], s[2:3], vcc
	v_cndmask_b32_e64 v8, 0, 1, s[2:3]
	v_cmp_ne_u32_e32 vcc, 0, v8
	s_cmp_eq_u64 vcc, 0
	s_cselect_b64 s[2:3], -1, 0
	v_cndmask_b32_e64 v8, 0, 1, s[2:3]
	s_nop 0
	v_readfirstlane_b32 s2, v8
	s_bitcmp0_b32 s2, 0
	s_cbranch_scc0 .LBB4_45
	s_cmp_lt_i32 s28, 4
	s_cbranch_scc1 .LBB4_46
	s_cmp_gt_i32 s28, 4
	s_cbranch_scc0 .LBB4_47
	s_mov_b64 s[4:5], -1
	v_mov_b32_e32 v8, 0
	s_cmp_gt_i32 s28, 5
	v_mov_b32_e32 v167, 0
	v_mov_b32_e32 v166, 0
	v_mov_b32_e32 v165, 0
	v_mov_b32_e32 v164, 0
	v_mov_b32_e32 v162, 0
	v_mov_b32_e32 v160, 0
	v_mov_b32_e32 v159, 0
	v_mov_b32_e32 v157, 0
	v_mov_b32_e32 v151, 0
	v_mov_b32_e32 v149, 0
	v_mov_b32_e32 v147, 0
	v_mov_b32_e32 v146, 0
	v_mov_b32_e32 v144, 0
	v_mov_b32_e32 v143, 0
	v_mov_b32_e32 v152, 0
	v_mov_b32_e32 v153, 0
	v_mov_b32_e32 v154, 0
	v_mov_b32_e32 v155, 0
	v_mov_b32_e32 v156, 0
	v_mov_b32_e32 v158, 0
	v_mov_b32_e32 v161, 0
	v_mov_b32_e32 v163, 0
	v_mov_b32_e32 v168, 0
	v_mov_b32_e32 v169, 0
	v_mov_b32_e32 v170, 0
	v_mov_b32_e32 v171, 0
	v_mov_b32_e32 v172, 0
	v_mov_b32_e32 v173, 0
	v_mov_b32_e32 v174, 0
	v_mov_b32_e32 v145, 0
	v_mov_b32_e32 v148, 0
	v_mov_b32_e32 v150, 0
	s_cbranch_scc0 .LBB4_50
	s_cmp_eq_u32 s28, 6
	s_cbranch_scc0 .LBB4_49
	v_mov_b32_e32 v145, 0
	v_mov_b32_e32 v148, 0
	v_mov_b32_e32 v150, 0
	v_mov_b32_e32 v143, 0
	v_mov_b32_e32 v144, 0
	v_mov_b32_e32 v146, 0
	v_mov_b32_e32 v147, 0
	v_mov_b32_e32 v149, 0
	v_mov_b32_e32 v151, 0
	v_mov_b32_e32 v152, 0
	v_mov_b32_e32 v153, 0
	v_mov_b32_e32 v154, 0
	v_mov_b32_e32 v155, 0
	v_mov_b32_e32 v156, 0
	v_mov_b32_e32 v158, 0
	v_mov_b32_e32 v161, 0
	v_mov_b32_e32 v163, 0
	v_mov_b32_e32 v157, 0
	v_mov_b32_e32 v159, 0
	v_mov_b32_e32 v160, 0
	v_mov_b32_e32 v162, 0
	v_mov_b32_e32 v164, 0
	v_mov_b32_e32 v165, 0
	v_mov_b32_e32 v166, 0
	v_mov_b32_e32 v167, 0
	v_mov_b32_e32 v168, 0
	v_mov_b32_e32 v169, 0
	v_mov_b32_e32 v170, 0
	v_mov_b32_e32 v171, 0
	v_mov_b32_e32 v172, 0
	v_mov_b32_e32 v173, 0
	v_mov_b32_e32 v174, 0
	v_fma_mix_f32 v148, v43, v7, v148 op_sel_hi:[1,0,0]
	v_fma_mix_f32 v150, v45, v7, v150 op_sel_hi:[1,0,0]
	v_fma_mix_f32 v143, v50, v7, v143 op_sel_hi:[1,0,0]
	v_fma_mix_f32 v144, v54, v7, v144 op_sel_hi:[1,0,0]
	v_fma_mix_f32 v146, v58, v7, v146 op_sel_hi:[1,0,0]
	v_fma_mix_f32 v147, v61, v7, v147 op_sel_hi:[1,0,0]
	v_fma_mix_f32 v149, v64, v7, v149 op_sel_hi:[1,0,0]
	v_fma_mix_f32 v151, v66, v7, v151 op_sel_hi:[1,0,0]
	v_fma_mix_f32 v152, v43, v7, v152 op_sel:[1,0,0] op_sel_hi:[1,0,0]
	v_fma_mix_f32 v153, v45, v7, v153 op_sel:[1,0,0] op_sel_hi:[1,0,0]
	v_fma_mix_f32 v154, v50, v7, v154 op_sel:[1,0,0] op_sel_hi:[1,0,0]
	v_fma_mix_f32 v155, v54, v7, v155 op_sel:[1,0,0] op_sel_hi:[1,0,0]
	v_fma_mix_f32 v156, v58, v7, v156 op_sel:[1,0,0] op_sel_hi:[1,0,0]
	v_fma_mix_f32 v158, v61, v7, v158 op_sel:[1,0,0] op_sel_hi:[1,0,0]
	v_fma_mix_f32 v161, v64, v7, v161 op_sel:[1,0,0] op_sel_hi:[1,0,0]
	v_fma_mix_f32 v163, v66, v7, v163 op_sel:[1,0,0] op_sel_hi:[1,0,0]
	v_fma_mix_f32 v157, v72, v7, v157 op_sel_hi:[1,0,0]
	v_fma_mix_f32 v159, v76, v7, v159 op_sel_hi:[1,0,0]
	v_fma_mix_f32 v160, v83, v7, v160 op_sel_hi:[1,0,0]
	v_fma_mix_f32 v162, v85, v7, v162 op_sel_hi:[1,0,0]
	v_fma_mix_f32 v164, v89, v7, v164 op_sel_hi:[1,0,0]
	v_fma_mix_f32 v165, v92, v7, v165 op_sel_hi:[1,0,0]
	v_fma_mix_f32 v166, v95, v7, v166 op_sel_hi:[1,0,0]
	v_fma_mix_f32 v167, v96, v7, v167 op_sel_hi:[1,0,0]
	v_fma_mix_f32 v168, v72, v7, v168 op_sel:[1,0,0] op_sel_hi:[1,0,0]
	v_fma_mix_f32 v169, v76, v7, v169 op_sel:[1,0,0] op_sel_hi:[1,0,0]
	v_fma_mix_f32 v170, v83, v7, v170 op_sel:[1,0,0] op_sel_hi:[1,0,0]
	v_fma_mix_f32 v171, v85, v7, v171 op_sel:[1,0,0] op_sel_hi:[1,0,0]
	v_fma_mix_f32 v172, v89, v7, v172 op_sel:[1,0,0] op_sel_hi:[1,0,0]
	v_fma_mix_f32 v173, v92, v7, v173 op_sel:[1,0,0] op_sel_hi:[1,0,0]
	v_fma_mix_f32 v174, v95, v7, v174 op_sel:[1,0,0] op_sel_hi:[1,0,0]
	v_fma_mix_f32 v145, v96, v7, v145 op_sel:[1,0,0] op_sel_hi:[1,0,0]
	s_branch .LBB4_50
